# forget-gate scan loop: dead denormal/inf range handling of log(1+exp(-|z|)) removed (argument is in [1,2]); bit-identical
# speedup vs baseline: 1.0064x; 1.0064x over previous
; __device__ __forceinline__ void p0_norm_gl(Frame& F) {
;     ...
;             const int c0 = F.tid, c1 = F.tid + 512; v2f wv[16];
; #pragma unroll
;             for (int r = 0; r < 16; ++r) wv[r] = (v2f){w2[r * KD + c0], w2[r * KD + c1]};
;             const v2f bv = (v2f){bgk[c0], bgk[c1]}; float cuma = 0.f, cumb = 0.f;
; #pragma unroll 2
;             for (int t = 0; t < CHK; ++t) {
;                 v2f z = bv;
; #pragma unroll
;                 for (int r = 0; r < 16; ++r) { const float g = glc[t * 16 + r]; z = __builtin_elementwise_fma(wv[r], (v2f){g, g}, z); }
;                 const float za = z.x, zb = z.y;
;                 const float la = fminf(za, 0.f) - __logf(1.0f + __expf(-fabsf(za))), lb = fminf(zb, 0.f) - __logf(1.0f + __expf(-fabsf(zb)));
;                 cuma += la * (1.0f / 16.0f); cumb += lb * (1.0f / 16.0f);
;                 BC[(size_t)(ch * CHK + t) * KD + c0] = cuma; BC[(size_t)(ch * CHK + t) * KD + c1] = cumb;
;             }
.LBB0_181:
	s_add_i32 s11, s45, 0
	v_mov_b32_e32 v144, s11
	ds_read_b128 v[38:41], v144 offset:34816
	ds_read_b128 v[42:45], v144 offset:34832
	ds_read_b128 v[46:49], v144 offset:34848
	ds_read_b128 v[50:53], v144 offset:34864
	ds_read_b128 v[54:57], v144 offset:34880
	ds_read_b128 v[58:61], v144 offset:34896
	ds_read_b128 v[62:65], v144 offset:34912
	ds_read_b128 v[144:147], v144 offset:34928
	s_waitcnt lgkmcnt(7)
	v_pk_fma_f32 v[162:163], v[2:3], v[38:39], v[34:35] op_sel_hi:[1,0,1]
	s_waitcnt lgkmcnt(3)
	v_pk_fma_f32 v[172:173], v[2:3], v[54:55], v[34:35] op_sel_hi:[1,0,1]
	v_pk_fma_f32 v[38:39], v[4:5], v[38:39], v[162:163] op_sel:[0,1,0]
	v_mov_b32_e32 v164, v41
	v_pk_fma_f32 v[54:55], v[4:5], v[54:55], v[172:173] op_sel:[0,1,0]
	v_pk_fma_f32 v[38:39], v[6:7], v[40:41], v[38:39] op_sel_hi:[1,0,1]
	v_mov_b32_e32 v174, v57
	v_pk_fma_f32 v[40:41], v[6:7], v[56:57], v[54:55] op_sel_hi:[1,0,1]
	v_pk_fma_f32 v[38:39], v[8:9], v[164:165], v[38:39] op_sel_hi:[1,0,1]
	v_pk_fma_f32 v[40:41], v[8:9], v[174:175], v[40:41] op_sel_hi:[1,0,1]
	v_pk_fma_f32 v[38:39], v[10:11], v[42:43], v[38:39] op_sel_hi:[1,0,1]
	s_waitcnt lgkmcnt(2)
	v_pk_fma_f32 v[40:41], v[10:11], v[58:59], v[40:41] op_sel_hi:[1,0,1]
	v_pk_fma_f32 v[38:39], v[12:13], v[42:43], v[38:39] op_sel:[0,1,0]
	v_mov_b32_e32 v166, v45
	v_pk_fma_f32 v[40:41], v[12:13], v[58:59], v[40:41] op_sel:[0,1,0]
	v_pk_fma_f32 v[38:39], v[14:15], v[44:45], v[38:39] op_sel_hi:[1,0,1]
	v_mov_b32_e32 v176, v61
	v_pk_fma_f32 v[40:41], v[14:15], v[60:61], v[40:41] op_sel_hi:[1,0,1]
	v_pk_fma_f32 v[38:39], v[16:17], v[166:167], v[38:39] op_sel_hi:[1,0,1]
	v_pk_fma_f32 v[40:41], v[16:17], v[176:177], v[40:41] op_sel_hi:[1,0,1]
	v_pk_fma_f32 v[38:39], v[18:19], v[46:47], v[38:39] op_sel_hi:[1,0,1]
	s_waitcnt lgkmcnt(1)
	v_pk_fma_f32 v[40:41], v[18:19], v[62:63], v[40:41] op_sel_hi:[1,0,1]
	v_pk_fma_f32 v[38:39], v[20:21], v[46:47], v[38:39] op_sel:[0,1,0]
	v_mov_b32_e32 v168, v49
	v_pk_fma_f32 v[40:41], v[20:21], v[62:63], v[40:41] op_sel:[0,1,0]
	v_pk_fma_f32 v[38:39], v[22:23], v[48:49], v[38:39] op_sel_hi:[1,0,1]
	v_mov_b32_e32 v178, v65
	v_pk_fma_f32 v[40:41], v[22:23], v[64:65], v[40:41] op_sel_hi:[1,0,1]
	v_pk_fma_f32 v[38:39], v[24:25], v[168:169], v[38:39] op_sel_hi:[1,0,1]
	v_pk_fma_f32 v[40:41], v[24:25], v[178:179], v[40:41] op_sel_hi:[1,0,1]
	v_pk_fma_f32 v[38:39], v[26:27], v[50:51], v[38:39] op_sel_hi:[1,0,1]
	s_waitcnt lgkmcnt(0)
	v_pk_fma_f32 v[40:41], v[26:27], v[144:145], v[40:41] op_sel_hi:[1,0,1]
	v_pk_fma_f32 v[38:39], v[28:29], v[50:51], v[38:39] op_sel:[0,1,0]
	v_mov_b32_e32 v170, v53
	v_pk_fma_f32 v[40:41], v[28:29], v[144:145], v[40:41] op_sel:[0,1,0]
	v_pk_fma_f32 v[38:39], v[30:31], v[52:53], v[38:39] op_sel_hi:[1,0,1]
	v_mov_b32_e32 v180, v147
	v_pk_fma_f32 v[40:41], v[30:31], v[146:147], v[40:41] op_sel_hi:[1,0,1]
	v_pk_fma_f32 v[38:39], v[32:33], v[170:171], v[38:39] op_sel_hi:[1,0,1]
	v_pk_fma_f32 v[40:41], v[32:33], v[180:181], v[40:41] op_sel_hi:[1,0,1]
	v_mul_f32_e64 v44, |v38|, s59
	v_mul_f32_e64 v45, |v39|, s59
	v_min_f32_e32 v43, 0, v38
	v_min_f32_e32 v42, 0, v39
	v_min_f32_e32 v39, 0, v40
	v_mul_f32_e64 v40, |v40|, s59
	v_min_f32_e32 v38, 0, v41
	v_mul_f32_e64 v41, |v41|, s59
	v_exp_f32_e32 v44, v44
	v_exp_f32_e32 v45, v45
	v_exp_f32_e32 v40, v40
	v_exp_f32_e32 v41, v41
	s_add_i32 s10, s46, 1
	s_ashr_i32 s11, s10, 31
	s_ashr_i32 s47, s46, 31
	s_lshl_b64 s[10:11], s[10:11], 12
	v_add_f32_e32 v44, 1.0, v44
	v_add_f32_e32 v45, 1.0, v45
	s_lshl_b64 s[12:13], s[46:47], 12
	v_lshl_add_u64 v[160:161], v[136:137], 0, s[10:11]
	v_add_f32_e32 v40, 1.0, v40
	v_add_f32_e32 v41, 1.0, v41
	v_lshl_add_u64 v[148:149], v[136:137], 0, s[12:13]
	v_log_f32_e32 v44, v44
	v_log_f32_e32 v45, v45
	v_log_f32_e32 v40, v40
	v_log_f32_e32 v41, v41
	v_mul_f32_e32 v50, 0x3f317217, v44
	v_mul_f32_e32 v51, 0x3f317217, v45
	v_mul_f32_e32 v52, 0x3f317217, v40
	v_mul_f32_e32 v53, 0x3f317217, v41
	v_fma_f32 v50, v44, s61, -v50
	v_fma_f32 v51, v45, s61, -v51
	v_fma_f32 v52, v40, s61, -v52
	v_fma_f32 v53, v41, s61, -v53
	v_fmac_f32_e32 v50, 0x3377d1cf, v44
	v_fmac_f32_e32 v51, 0x3377d1cf, v45
	v_fmac_f32_e32 v52, 0x3377d1cf, v40
	v_fmac_f32_e32 v53, 0x3377d1cf, v41
	v_fmac_f32_e32 v50, 0x3f317217, v44
	v_fmac_f32_e32 v51, 0x3f317217, v45
	v_fmac_f32_e32 v52, 0x3f317217, v40
	v_fmac_f32_e32 v53, 0x3f317217, v41
	v_pk_add_f32 v[40:41], v[42:43], v[50:51] op_sel:[0,1] op_sel_hi:[1,0] neg_lo:[0,1] neg_hi:[0,1]
	s_addk_i32 s45, 0x80
	s_add_i32 s46, s46, 2
	v_pk_add_f32 v[38:39], v[38:39], v[52:53] op_sel:[0,1] op_sel_hi:[1,0] neg_lo:[0,1] neg_hi:[0,1]
	v_pk_fma_f32 v[36:37], v[40:41], s[42:43], v[36:37] op_sel_hi:[1,0,1]
	s_cmpk_lg_i32 s45, 0x1000
	global_store_dword v[148:149], v37, off
	global_store_dword v[148:149], v36, off offset:2048
	v_pk_fma_f32 v[36:37], v[38:39], s[42:43], v[36:37] op_sel_hi:[1,0,1]
	global_store_dword v[160:161], v37, off
	global_store_dword v[160:161], v36, off offset:2048
	s_cbranch_scc1 .LBB0_181
	s_add_i32 s44, s44, s34
	s_add_i32 s3, s3, s35
	v_lshl_add_u64 v[140:141], v[140:141], 0, s[24:25]
	s_cmpk_lt_i32 s44, 0x100
	v_lshl_add_u64 v[142:143], v[142:143], 0, s[26:27]
	s_barrier
	s_cbranch_scc1 .LBB0_166
